# attention QK^T blocks (dilated and MoBA): the four K-fragment ds_reads of a block issued together into spare registers with counted lgkmcnt waits (were read+lgkmcnt(0)+MFMA in series)
# baseline (speedup 1.0000x reference)
.LBB0_251:
	s_or_b64 exec, exec, s[0:1]
	s_mul_hi_i32 s0, s33, 0x2aaaaaab
	s_lshr_b32 s1, s0, 31
	s_ashr_i32 s0, s0, 4
	s_add_i32 s25, s0, s1
	s_and_b32 s31, s25, 15
	s_add_i32 s0, s31, 1
	v_cvt_f32_ubyte0_e32 v24, s0
	v_mul_f32_e32 v18, -0.5, v24
	s_mov_b32 s0, 0xc2fc0000
	v_cmp_gt_f32_e32 vcc, s0, v18
	s_and_b64 s[0:1], vcc, exec
	s_cselect_b32 s36, 0xffffffc0, 0
	s_and_b64 s[0:1], s[16:17], exec
	s_cselect_b32 s16, 4, 16
	s_and_b64 s[0:1], s[18:19], exec
	s_cselect_b32 s19, 1, s16
	s_add_i32 s15, s15, s3
	s_lshl_b32 s0, s25, 9
	v_add_u32_e32 v30, s15, v160
	s_and_b32 s0, s0, 0xffffe000
	v_lshlrev_b32_e32 v18, s34, v30
	s_or_b32 s0, s35, s0
	v_add_u32_e32 v158, s0, v18
	v_mov_b64_e32 v[18:19], s[12:13]
	s_movk_i32 s39, 0x4800
	v_mad_i64_i32 v[18:19], s[0:1], v158, s39, v[18:19]
	s_mul_i32 s0, s14, 0xc00
	s_ashr_i32 s1, s0, 31
	s_lshl_b32 s56, s31, 7
	s_add_i32 s18, s33, s2
	s_cmpk_gt_i32 s18, 0xbff
	v_lshl_add_u64 v[18:19], s[0:1], 1, v[18:19]
	s_cselect_b64 s[0:1], -1, 0
	s_cmpk_lt_i32 s18, 0xc00
	s_cselect_b32 s16, s18, s33
	s_ashr_i32 s17, s16, 5
	s_mul_hi_i32 s25, s17, 0x55555556
	s_lshr_b32 s33, s25, 31
	s_add_i32 s25, s25, s33
	s_mul_i32 s25, s25, 3
	s_sub_i32 s17, s17, s25
	s_mul_hi_i32 s25, s16, 0x2aaaaaab
	s_lshr_b32 s33, s25, 31
	s_ashr_i32 s25, s25, 4
	s_add_i32 s25, s25, s33
	s_cmp_eq_u32 s17, 1
	s_cselect_b32 s33, 2, 4
	s_cmp_lg_u32 s17, 0
	s_cselect_b32 s33, s33, 0
	s_lshl_b32 s16, s16, 8
	s_and_b32 s16, s16, 0x1f00
	s_sub_i32 s34, 13, s33
	s_lshr_b32 s37, s16, s34
	s_lshl_b32 s34, s37, s34
	s_sub_i32 s16, s16, s34
	s_add_i32 s38, s16, 0xffffff80
	s_lshl_b32 s16, s25, 9
	s_and_b32 s16, s16, 0xffffe000
	s_mul_hi_i32 s34, s16, 0x4800
	s_mulk_i32 s16, 0x4800
	s_add_u32 s35, s12, s16
	s_mul_i32 s16, s17, 0xc00
	v_lshl_add_u64 v[18:19], v[18:19], 0, s[56:57]
	s_addc_u32 s34, s13, s34
	s_ashr_i32 s17, s16, 31
	v_lshl_add_u64 v[18:19], v[18:19], 0, v[0:1]
	v_mov_b32_e32 v26, v155
	s_lshl_b64 s[16:17], s[16:17], 1
	s_waitcnt vmcnt(0) lgkmcnt(0)
	s_barrier
	s_add_u32 s16, s35, s16
	v_add_u32_e32 v27, 0x200, v26
	s_addc_u32 s17, s34, s17
	s_lshl_b32 s25, s25, 7
	v_ashrrev_i32_e32 v20, 3, v26
	v_ashrrev_i32_e32 v22, 3, v27
	s_and_b32 s25, s25, 0x780
	v_add_u32_e32 v20, s38, v20
	v_add_u32_e32 v22, s38, v22
	s_add_u32 s34, s16, s25
	v_lshlrev_b32_e32 v18, 4, v26
	v_max_i32_e32 v20, 0, v20
	v_max_i32_e32 v22, 0, v22
	s_addc_u32 s35, s17, 0
	v_and_b32_e32 v18, 0x70, v18
	v_mov_b32_e32 v19, v1
	v_lshlrev_b32_e32 v20, s33, v20
	v_lshlrev_b32_e32 v22, s33, v22
	s_add_u32 s16, s34, 0x800
	v_lshl_add_u64 v[18:19], s[34:35], 0, v[18:19]
	v_add_u32_e32 v20, s37, v20
	v_add_u32_e32 v22, s37, v22
	s_addc_u32 s17, s35, 0
	v_mad_u64_u32 v[20:21], s[34:35], v20, s39, v[18:19]
	v_mad_u64_u32 v[22:23], s[34:35], v22, s39, v[18:19]
	global_load_dwordx4 v[106:109], v[20:21], off offset:2048
	global_load_dwordx4 v[98:101], v[22:23], off offset:2048
	v_add_u32_e32 v20, 0x400, v26
	v_add_u32_e32 v22, 0x600, v26
	v_ashrrev_i32_e32 v20, 3, v20
	v_ashrrev_i32_e32 v22, 3, v22
	v_add_u32_e32 v20, s38, v20
	v_add_u32_e32 v22, s38, v22
	v_max_i32_e32 v20, 0, v20
	v_max_i32_e32 v22, 0, v22
	v_lshlrev_b32_e32 v20, s33, v20
	v_lshlrev_b32_e32 v22, s33, v22
	v_add_u32_e32 v20, s37, v20
	v_add_u32_e32 v22, s37, v22
	v_mad_u64_u32 v[20:21], s[34:35], v20, s39, v[18:19]
	v_mad_u64_u32 v[22:23], s[34:35], v22, s39, v[18:19]
	global_load_dwordx4 v[114:117], v[20:21], off offset:2048
	global_load_dwordx4 v[102:105], v[22:23], off offset:2048
	v_add_u32_e32 v20, 0x800, v26
	v_add_u32_e32 v22, 0xa00, v26
	v_ashrrev_i32_e32 v20, 3, v20
	v_ashrrev_i32_e32 v22, 3, v22
	v_add_u32_e32 v20, s38, v20
	v_add_u32_e32 v22, s38, v22
	v_max_i32_e32 v20, 0, v20
	v_max_i32_e32 v22, 0, v22
	v_lshlrev_b32_e32 v20, s33, v20
	v_lshlrev_b32_e32 v22, s33, v22
	v_add_u32_e32 v20, s37, v20
	v_add_u32_e32 v22, s37, v22
	v_mad_u64_u32 v[20:21], s[34:35], v20, s39, v[18:19]
	v_mad_u64_u32 v[18:19], s[34:35], v22, s39, v[18:19]
	s_movk_i32 s25, 0x300
	v_cndmask_b32_e32 v25, 0, v224, vcc
	global_load_dwordx4 v[118:121], v[20:21], off offset:2048
	global_load_dwordx4 v[110:113], v[18:19], off offset:2048
	v_add_u32_e32 v18, 0xfffffe00, v26
	v_cmp_gt_i32_e32 vcc, s25, v26
	s_movk_i32 s25, 0x100
	v_fmac_f32_e32 v25, -0.5, v24
	v_cndmask_b32_e32 v18, v18, v26, vcc
	v_ashrrev_i32_e32 v19, 1, v18
	v_and_b32_e32 v19, -4, v19
	v_add_u32_e32 v19, s38, v19
	v_max_i32_e32 v28, 0, v19
	v_lshlrev_b32_e32 v18, 4, v18
	v_and_b32_e32 v18, 0x70, v18
	v_mov_b32_e32 v19, v1
	v_lshlrev_b32_e32 v20, s33, v28
	v_add_lshl_u32 v22, v28, 1, s33
	v_lshl_add_u64 v[18:19], s[16:17], 0, v[18:19]
	v_add_u32_e32 v20, s37, v20
	v_add_u32_e32 v22, s37, v22
	v_mad_u64_u32 v[20:21], s[34:35], v20, s39, v[18:19]
	v_mad_u64_u32 v[22:23], s[34:35], v22, s39, v[18:19]
	global_load_dwordx4 v[82:85], v[20:21], off offset:2048
	global_load_dwordx4 v[86:89], v[22:23], off offset:2048
	v_add_lshl_u32 v20, v28, 2, s33
	v_add_lshl_u32 v22, v28, 3, s33
	v_add_u32_e32 v20, s37, v20
	v_add_u32_e32 v22, s37, v22
	v_mad_u64_u32 v[20:21], s[34:35], v20, s39, v[18:19]
	v_mad_u64_u32 v[18:19], s[34:35], v22, s39, v[18:19]
	v_cmp_gt_i32_e32 vcc, s25, v26
	global_load_dwordx4 v[90:93], v[20:21], off offset:2048
	global_load_dwordx4 v[94:97], v[18:19], off offset:2048
	v_cndmask_b32_e32 v18, v26, v27, vcc
	v_ashrrev_i32_e32 v19, 1, v18
	v_and_b32_e32 v19, -4, v19
	v_add_u32_e32 v19, s38, v19
	v_max_i32_e32 v26, 0, v19
	v_lshlrev_b32_e32 v18, 4, v18
	v_and_b32_e32 v18, 0x70, v18
	v_mov_b32_e32 v19, v1
	v_lshlrev_b32_e32 v20, s33, v26
	v_lshl_add_u64 v[18:19], s[16:17], 0, v[18:19]
	v_add_u32_e32 v20, s37, v20
	v_add_lshl_u32 v22, v26, 1, s33
	v_mad_u64_u32 v[20:21], s[16:17], v20, s39, v[18:19]
	v_add_u32_e32 v22, s37, v22
	v_mad_u64_u32 v[22:23], s[16:17], v22, s39, v[18:19]
	global_load_dwordx4 v[66:69], v[20:21], off offset:2048
	global_load_dwordx4 v[70:73], v[22:23], off offset:2048
	v_add_lshl_u32 v20, v26, 2, s33
	v_add_u32_e32 v20, s37, v20
	v_add_lshl_u32 v22, v26, 3, s33
	v_mad_u64_u32 v[20:21], s[16:17], v20, s39, v[18:19]
	v_add_u32_e32 v22, s37, v22
	v_mad_u64_u32 v[18:19], s[16:17], v22, s39, v[18:19]
	global_load_dwordx4 v[74:77], v[20:21], off offset:2048
	global_load_dwordx4 v[78:81], v[18:19], off offset:2048
	ds_read_b128 v[18:21], v162
	v_exp_f32_e32 v22, v25
	v_cvt_f32_ubyte0_e32 v23, s19
	s_sub_i32 s16, 0x80, s15
	s_ashr_i32 s16, s16, 5
	v_ldexp_f32 v22, v22, s36
	v_mul_f32_e32 v22, 0x3fb8aa3b, v22
	v_mul_f32_e32 v157, v22, v23
	ds_read_b128 v[22:25], v162 offset:32
	s_waitcnt lgkmcnt(1)
	v_mfma_f32_32x32x16_bf16 v[50:65], v[18:21], v[134:137], 0
	ds_read_b128 v[18:21], v162 offset:64
	ds_read_b128 v[26:29], v162 offset:96
	s_cmpk_lt_i32 s15, 0x80
	s_cselect_b32 s17, s16, 0
	s_cmp_gt_i32 s17, 4
	v_sub_u32_e32 v188, v30, v154
	s_waitcnt lgkmcnt(2)
	v_mfma_f32_32x32x16_bf16 v[50:65], v[22:25], v[130:133], v[50:65]
	s_waitcnt lgkmcnt(1)
	v_mfma_f32_32x32x16_bf16 v[50:65], v[18:21], v[126:129], v[50:65]
	s_waitcnt lgkmcnt(0)
	v_mfma_f32_32x32x16_bf16 v[50:65], v[26:29], v[122:125], v[50:65]
	s_cbranch_scc1 .LBB0_260
	s_cmp_eq_u32 s17, 4
	s_cbranch_scc1 .LBB0_254
	ds_read_b128 v[2:5], v163
	ds_read_b128 v[18:21], v163 offset:32
	ds_read_b128 v[200:203], v163 offset:64
	ds_read_b128 v[204:207], v163 offset:96
	s_waitcnt lgkmcnt(3)
	v_mfma_f32_32x32x16_bf16 v[2:17], v[2:5], v[134:137], 0
	s_waitcnt lgkmcnt(2)
	v_mfma_f32_32x32x16_bf16 v[2:17], v[18:21], v[130:133], v[2:17]
	s_waitcnt lgkmcnt(1)
	v_mfma_f32_32x32x16_bf16 v[2:17], v[200:203], v[126:129], v[2:17]
	s_waitcnt lgkmcnt(0)
	v_mfma_f32_32x32x16_bf16 v[2:17], v[204:207], v[122:125], v[2:17]

.LBB0_256:
	s_cmp_eq_u32 s17, 2
	s_cbranch_scc1 .LBB0_258
	ds_read_b128 v[2:5], v165
	ds_read_b128 v[138:141], v165 offset:32
	ds_read_b128 v[200:203], v165 offset:64
	ds_read_b128 v[204:207], v165 offset:96
	s_waitcnt lgkmcnt(3)
	v_mfma_f32_32x32x16_bf16 v[2:17], v[2:5], v[134:137], 0
	s_waitcnt lgkmcnt(2)
	v_mfma_f32_32x32x16_bf16 v[2:17], v[138:141], v[130:133], v[2:17]
	s_waitcnt lgkmcnt(1)
	v_mfma_f32_32x32x16_bf16 v[2:17], v[200:203], v[126:129], v[2:17]
	s_waitcnt lgkmcnt(0)
	v_mfma_f32_32x32x16_bf16 v[2:17], v[204:207], v[122:125], v[2:17]

.LBB0_261:
	s_cmp_eq_u32 s17, 3
	s_cbranch_scc1 .LBB0_263
	ds_read_b128 v[50:53], v164
	ds_read_b128 v[138:141], v164 offset:32
	ds_read_b128 v[200:203], v164 offset:64
	ds_read_b128 v[204:207], v164 offset:96
	s_waitcnt lgkmcnt(3)
	v_mfma_f32_32x32x16_bf16 v[50:65], v[50:53], v[134:137], 0
	s_waitcnt lgkmcnt(2)
	v_mfma_f32_32x32x16_bf16 v[50:65], v[138:141], v[130:133], v[50:65]
	s_waitcnt lgkmcnt(1)
	v_mfma_f32_32x32x16_bf16 v[50:65], v[200:203], v[126:129], v[50:65]
	s_waitcnt lgkmcnt(0)
	v_mfma_f32_32x32x16_bf16 v[50:65], v[204:207], v[122:125], v[50:65]

.LBB0_265:
	s_cmp_eq_u32 s17, 1
	s_cbranch_scc1 .LBB0_267
	ds_read_b128 v[50:53], v166
	ds_read_b128 v[138:141], v166 offset:32
	ds_read_b128 v[200:203], v166 offset:64
	ds_read_b128 v[204:207], v166 offset:96
	s_waitcnt lgkmcnt(3)
	v_mfma_f32_32x32x16_bf16 v[50:65], v[50:53], v[134:137], 0
	s_waitcnt lgkmcnt(2)
	v_mfma_f32_32x32x16_bf16 v[50:65], v[138:141], v[130:133], v[50:65]
	s_waitcnt lgkmcnt(1)
	v_mfma_f32_32x32x16_bf16 v[50:65], v[200:203], v[126:129], v[50:65]
	s_waitcnt lgkmcnt(0)
	v_mfma_f32_32x32x16_bf16 v[50:65], v[204:207], v[122:125], v[50:65]

.LBB0_268:
	s_cmp_gt_i32 s17, -1
	s_cbranch_scc1 .LBB0_270
	ds_read_b128 v[2:5], v167
	ds_read_b128 v[200:203], v167 offset:32
	ds_read_b128 v[204:207], v167 offset:64
	ds_read_b128 v[208:211], v167 offset:96
	s_waitcnt lgkmcnt(3)
	v_mfma_f32_32x32x16_bf16 v[2:17], v[2:5], v[134:137], 0
	s_waitcnt lgkmcnt(2)
	v_mfma_f32_32x32x16_bf16 v[2:17], v[200:203], v[130:133], v[2:17]
	s_waitcnt lgkmcnt(1)
	v_mfma_f32_32x32x16_bf16 v[2:17], v[204:207], v[126:129], v[2:17]
	s_waitcnt lgkmcnt(0)
	v_mfma_f32_32x32x16_bf16 v[2:17], v[208:211], v[122:125], v[2:17]

.LBB0_798:
	s_add_i32 s25, s35, -1
	s_cmp_lt_i32 s25, s29
	s_cselect_b64 s[18:19], -1, 0
	s_cmp_ge_i32 s25, s29
	s_cbranch_scc1 .LBB0_800
	s_waitcnt lgkmcnt(2)
	ds_read_b128 v[2:5], v203
	ds_read_b128 v[6:9], v203 offset:32
	ds_read_b128 v[10:13], v203 offset:64
	ds_read_b128 v[128:131], v203 offset:96
	s_waitcnt lgkmcnt(3)
	v_mfma_f32_32x32x16_bf16 v[16:31], v[2:5], v[112:115], 0
	s_waitcnt lgkmcnt(2)
	v_mfma_f32_32x32x16_bf16 v[16:31], v[6:9], v[116:119], v[16:31]
	s_waitcnt lgkmcnt(1)
	v_mfma_f32_32x32x16_bf16 v[16:31], v[10:13], v[120:123], v[16:31]
	s_waitcnt lgkmcnt(0)
	v_mfma_f32_32x32x16_bf16 v[16:31], v[128:131], v[124:127], v[16:31]

.LBB0_803:
	s_cmp_ge_i32 s35, s29
	s_cbranch_scc1 .LBB0_805
	s_waitcnt lgkmcnt(2)
	ds_read_b128 v[2:5], v203 offset:4608
	ds_read_b128 v[6:9], v203 offset:4640
	ds_read_b128 v[10:13], v203 offset:4672
	ds_read_b128 v[128:131], v203 offset:4704
	s_waitcnt lgkmcnt(3)
	v_mfma_f32_32x32x16_bf16 v[32:47], v[2:5], v[112:115], 0
	s_waitcnt lgkmcnt(2)
	v_mfma_f32_32x32x16_bf16 v[32:47], v[6:9], v[116:119], v[32:47]
	s_waitcnt lgkmcnt(1)
	v_mfma_f32_32x32x16_bf16 v[32:47], v[10:13], v[120:123], v[32:47]
	s_waitcnt lgkmcnt(0)
	v_mfma_f32_32x32x16_bf16 v[32:47], v[128:131], v[124:127], v[32:47]
